# attention row-max: drop NaN-quieting v_max x,x and fold 8-way max into v_max3 (7 of 18 sites) + lane-exchange max (36 sites)
# speedup vs baseline: 1.0008x; 1.0008x over previous
.LBB0_749:
	s_add_i32 s29, s18, 3
	s_min_i32 s29, s29, 11
	s_add_i32 s29, s29, s28
	s_waitcnt vmcnt(18)
	v_med3_i32 v54, s29, 0, v184
	v_lshl_or_b32 v2, v54, 11, v160
	v_lshl_add_u64 v[4:5], v[104:105], 0, v[2:3]
	v_lshlrev_b32_e32 v2, 12, v54
	global_load_dwordx4 v[46:49], v[4:5], off
	global_load_dwordx4 v[50:53], v[4:5], off offset:1024
	v_lshl_add_u64 v[4:5], v[106:107], 0, v[2:3]
	global_load_dwordx4 v[54:57], v[4:5], off
	global_load_dwordx4 v[58:61], v[4:5], off offset:1024
	global_load_dwordx4 v[62:65], v[4:5], off offset:2048
	global_load_dwordx4 v[66:69], v[4:5], off offset:3072
	s_add_i32 s29, s15, s18
	s_cmpk_gt_u32 s29, 0xff
	s_cbranch_scc1 .LBB0_755
	s_waitcnt vmcnt(14)
	ds_read2_b32 v[94:95], v108 offset0:8 offset1:9
	ds_read2_b32 v[96:97], v108 offset0:10 offset1:11
	ds_read2_b32 v[116:117], v108 offset0:24 offset1:25
	ds_read2_b32 v[118:119], v108 offset0:26 offset1:27
	s_waitcnt vmcnt(11) lgkmcnt(2)
	v_mfma_f32_16x16x32_fp8_fp8 v[94:97], v[90:91], v[38:39], v[94:97]
	v_mfma_f32_16x16x32_fp8_fp8 v[98:101], v[92:93], v[40:41], v[94:97]
	s_waitcnt vmcnt(10) lgkmcnt(0)
	v_mfma_f32_16x16x32_fp8_fp8 v[94:97], v[86:87], v[38:39], v[116:119]
	v_mfma_f32_16x16x32_fp8_fp8 v[94:97], v[88:89], v[40:41], v[94:97]
	s_nop 4
	v_max3_f32 v2, v98, v99, v100
	v_max_f32_e32 v2, v2, v101
	s_nop 3
	v_max3_f32 v5, v95, v96, v97
	v_max3_f32 v2, v2, v94, v5
	v_mov_b32_e32 v4, v2
	s_nop 1
	v_permlane16_swap_b32_e32 v2, v4
	v_max_f32_e32 v2, v2, v4
	v_mov_b32_e32 v4, v2
	s_nop 1
	v_permlane32_swap_b32_e32 v2, v4
	v_max_f32_e32 v2, v2, v4
	v_cmp_gt_f32_e32 vcc, v2, v112
	s_cbranch_vccz .LBB0_752
	v_max_f32_e32 v2, v2, v2
	v_max_f32_e32 v4, v112, v112
	v_max_f32_e32 v4, v4, v2
	v_sub_f32_e32 v2, v112, v4
	v_exp_f32_e32 v2, v2
	v_mov_b32_e32 v112, v4
	v_mul_f32_e32 v113, v113, v2
	v_pk_mul_f32 v[36:37], v[36:37], v[2:3] op_sel_hi:[1,0]
	v_pk_mul_f32 v[34:35], v[34:35], v[2:3] op_sel_hi:[1,0]
	v_pk_mul_f32 v[32:33], v[32:33], v[2:3] op_sel_hi:[1,0]
	v_pk_mul_f32 v[30:31], v[30:31], v[2:3] op_sel_hi:[1,0]
	v_pk_mul_f32 v[28:29], v[28:29], v[2:3] op_sel_hi:[1,0]
	v_pk_mul_f32 v[26:27], v[26:27], v[2:3] op_sel_hi:[1,0]
	v_pk_mul_f32 v[24:25], v[24:25], v[2:3] op_sel_hi:[1,0]
	v_pk_mul_f32 v[22:23], v[22:23], v[2:3] op_sel_hi:[1,0]
.LBB0_752:
	v_sub_f32_e32 v2, v98, v112
	v_sub_f32_e32 v4, v99, v112
	v_sub_f32_e32 v5, v100, v112
	v_sub_f32_e32 v98, v101, v112
	v_sub_f32_e32 v94, v94, v112
	v_sub_f32_e32 v95, v95, v112
	v_sub_f32_e32 v96, v96, v112
	v_sub_f32_e32 v97, v97, v112
	v_exp_f32_e32 v2, v2
	v_exp_f32_e32 v4, v4
	v_exp_f32_e32 v5, v5
	v_exp_f32_e32 v98, v98
	v_exp_f32_e32 v94, v94
	v_exp_f32_e32 v95, v95
	v_exp_f32_e32 v96, v96
	v_exp_f32_e32 v97, v97
	v_cvt_pk_bf16_f32 v116, v2, v4
	v_cvt_pk_bf16_f32 v117, v5, v98
	v_cvt_pk_bf16_f32 v118, v94, v95
	v_cvt_pk_bf16_f32 v119, v96, v97
	s_waitcnt vmcnt(9)
	s_nop 0
	v_mfma_f32_16x16x32_bf16 v[34:37], v[82:85], v[116:119], v[34:37]
	s_waitcnt vmcnt(8)
	v_mfma_f32_16x16x32_bf16 v[30:33], v[78:81], v[116:119], v[30:33]
	s_waitcnt vmcnt(7)
	v_mfma_f32_16x16x32_bf16 v[26:29], v[74:77], v[116:119], v[26:29]
	s_waitcnt vmcnt(6)
	v_mfma_f32_16x16x32_bf16 v[22:25], v[70:73], v[116:119], v[22:25]
	ds_read2_b32 v[116:117], v108 offset1:1
	ds_read2_b32 v[118:119], v108 offset0:2 offset1:3
	ds_read2_b32 v[120:121], v108 offset0:16 offset1:17
	ds_read2_b32 v[122:123], v108 offset0:18 offset1:19
	s_waitcnt lgkmcnt(2)
	v_mfma_f32_16x16x32_fp8_fp8 v[116:119], v[90:91], v[42:43], v[116:119]
	v_mfma_f32_16x16x32_fp8_fp8 v[90:93], v[92:93], v[44:45], v[116:119]
	s_waitcnt lgkmcnt(0)
	v_mfma_f32_16x16x32_fp8_fp8 v[116:119], v[86:87], v[42:43], v[120:123]
	v_mfma_f32_16x16x32_fp8_fp8 v[86:89], v[88:89], v[44:45], v[116:119]
	s_nop 4
	v_max3_f32 v99, v90, v91, v92
	v_max_f32_e32 v99, v99, v93
	s_nop 3
	v_max3_f32 v101, v87, v88, v89
	v_max3_f32 v99, v99, v86, v101
	v_mov_b32_e32 v100, v99
	s_nop 1
	v_permlane16_swap_b32_e32 v99, v100
	v_max_f32_e32 v99, v99, v100
	v_mov_b32_e32 v100, v99
	s_nop 1
	v_permlane32_swap_b32_e32 v99, v100
	v_max_f32_e32 v99, v99, v100
	v_cmp_gt_f32_e32 vcc, v99, v114
	s_cbranch_vccz .LBB0_754
	v_max_f32_e32 v99, v99, v99
	v_max_f32_e32 v100, v114, v114
	v_max_f32_e32 v99, v100, v99
	v_sub_f32_e32 v100, v114, v99
	v_exp_f32_e32 v100, v100
	v_mov_b32_e32 v114, v99
	v_mul_f32_e32 v115, v115, v100
	v_pk_mul_f32 v[20:21], v[20:21], v[100:101] op_sel_hi:[1,0]
	v_pk_mul_f32 v[18:19], v[18:19], v[100:101] op_sel_hi:[1,0]
	v_pk_mul_f32 v[16:17], v[16:17], v[100:101] op_sel_hi:[1,0]
	v_pk_mul_f32 v[14:15], v[14:15], v[100:101] op_sel_hi:[1,0]
	v_pk_mul_f32 v[12:13], v[12:13], v[100:101] op_sel_hi:[1,0]
	v_pk_mul_f32 v[10:11], v[10:11], v[100:101] op_sel_hi:[1,0]
	v_pk_mul_f32 v[8:9], v[8:9], v[100:101] op_sel_hi:[1,0]
	v_pk_mul_f32 v[6:7], v[6:7], v[100:101] op_sel_hi:[1,0]

.LBB0_758:
	s_min_i32 s6, s15, 5
	s_add_i32 s6, s6, s11
	s_waitcnt vmcnt(11)
	v_med3_i32 v54, s6, 0, 63
	v_lshl_or_b32 v2, v54, 11, v160
	v_lshl_add_u64 v[50:51], v[104:105], 0, v[2:3]
	v_lshlrev_b32_e32 v2, 12, v54
	s_waitcnt vmcnt(8)
	v_lshl_add_u64 v[66:67], v[106:107], 0, v[2:3]
	global_load_dwordx4 v[46:49], v[50:51], off
	s_nop 0
	global_load_dwordx4 v[50:53], v[50:51], off offset:1024
	s_nop 0
	global_load_dwordx4 v[54:57], v[66:67], off
	global_load_dwordx4 v[58:61], v[66:67], off offset:1024
	global_load_dwordx4 v[62:65], v[66:67], off offset:2048
	s_nop 0
	global_load_dwordx4 v[66:69], v[66:67], off offset:3072
	s_add_i32 s6, s10, s15
	s_add_i32 s6, s6, -3
	s_cmp_gt_u32 s6, 63
	s_cbranch_scc1 .LBB0_764
	ds_read2_b32 v[94:95], v5 offset1:1
	ds_read2_b32 v[96:97], v5 offset0:2 offset1:3
	ds_read2_b32 v[108:109], v5 offset0:16 offset1:17
	ds_read2_b32 v[110:111], v5 offset0:18 offset1:19
	s_waitcnt vmcnt(11) lgkmcnt(2)
	v_mfma_f32_16x16x32_fp8_fp8 v[94:97], v[90:91], v[38:39], v[94:97]
	v_mfma_f32_16x16x32_fp8_fp8 v[98:101], v[92:93], v[40:41], v[94:97]
	s_waitcnt vmcnt(10) lgkmcnt(0)
	v_mfma_f32_16x16x32_fp8_fp8 v[94:97], v[86:87], v[38:39], v[108:111]
	v_mfma_f32_16x16x32_fp8_fp8 v[94:97], v[88:89], v[40:41], v[94:97]
	s_nop 4
	v_max3_f32 v2, v98, v99, v100
	v_max_f32_e32 v2, v2, v101
	s_nop 3
	v_max3_f32 v109, v95, v96, v97
	v_max3_f32 v2, v2, v94, v109
	v_mov_b32_e32 v108, v2
	s_nop 1
	v_permlane16_swap_b32_e32 v2, v108
	v_max_f32_e32 v2, v2, v108
	v_mov_b32_e32 v108, v2
	s_nop 1
	v_permlane32_swap_b32_e32 v2, v108
	v_max_f32_e32 v2, v2, v108
	v_cmp_gt_f32_e32 vcc, v2, v112
	s_cbranch_vccz .LBB0_761
	v_max_f32_e32 v2, v2, v2
	v_max_f32_e32 v108, v112, v112
	v_max_f32_e32 v108, v108, v2
	v_sub_f32_e32 v2, v112, v108
	v_exp_f32_e32 v2, v2
	v_mov_b32_e32 v112, v108
	v_mul_f32_e32 v113, v113, v2
	v_pk_mul_f32 v[36:37], v[36:37], v[2:3] op_sel_hi:[1,0]
	v_pk_mul_f32 v[34:35], v[34:35], v[2:3] op_sel_hi:[1,0]
	v_pk_mul_f32 v[32:33], v[32:33], v[2:3] op_sel_hi:[1,0]
	v_pk_mul_f32 v[30:31], v[30:31], v[2:3] op_sel_hi:[1,0]
	v_pk_mul_f32 v[28:29], v[28:29], v[2:3] op_sel_hi:[1,0]
	v_pk_mul_f32 v[26:27], v[26:27], v[2:3] op_sel_hi:[1,0]
	v_pk_mul_f32 v[24:25], v[24:25], v[2:3] op_sel_hi:[1,0]
	v_pk_mul_f32 v[22:23], v[22:23], v[2:3] op_sel_hi:[1,0]
.LBB0_761:
	v_sub_f32_e32 v2, v98, v112
	v_sub_f32_e32 v98, v99, v112
	v_sub_f32_e32 v99, v100, v112
	v_sub_f32_e32 v100, v101, v112
	v_sub_f32_e32 v94, v94, v112
	v_sub_f32_e32 v95, v95, v112
	v_sub_f32_e32 v96, v96, v112
	v_sub_f32_e32 v97, v97, v112
	v_exp_f32_e32 v2, v2
	v_exp_f32_e32 v98, v98
	v_exp_f32_e32 v99, v99
	v_exp_f32_e32 v100, v100
	v_exp_f32_e32 v94, v94
	v_exp_f32_e32 v95, v95
	v_exp_f32_e32 v96, v96
	v_exp_f32_e32 v97, v97
	v_cvt_pk_bf16_f32 v108, v2, v98
	v_cvt_pk_bf16_f32 v109, v99, v100
	v_cvt_pk_bf16_f32 v110, v94, v95
	v_cvt_pk_bf16_f32 v111, v96, v97
	s_waitcnt vmcnt(9)
	s_nop 0
	v_mfma_f32_16x16x32_bf16 v[34:37], v[82:85], v[108:111], v[34:37]
	s_waitcnt vmcnt(8)
	v_mfma_f32_16x16x32_bf16 v[30:33], v[78:81], v[108:111], v[30:33]
	s_waitcnt vmcnt(7)
	v_mfma_f32_16x16x32_bf16 v[26:29], v[74:77], v[108:111], v[26:29]
	s_waitcnt vmcnt(6)
	v_mfma_f32_16x16x32_bf16 v[22:25], v[70:73], v[108:111], v[22:25]
	ds_read2_b32 v[108:109], v103 offset1:1
	ds_read2_b32 v[110:111], v103 offset0:2 offset1:3
	ds_read2_b32 v[116:117], v103 offset0:16 offset1:17
	ds_read2_b32 v[118:119], v103 offset0:18 offset1:19
	s_waitcnt lgkmcnt(2)
	v_mfma_f32_16x16x32_fp8_fp8 v[108:111], v[90:91], v[42:43], v[108:111]
	v_mfma_f32_16x16x32_fp8_fp8 v[90:93], v[92:93], v[44:45], v[108:111]
	s_waitcnt lgkmcnt(0)
	v_mfma_f32_16x16x32_fp8_fp8 v[108:111], v[86:87], v[42:43], v[116:119]
	v_mfma_f32_16x16x32_fp8_fp8 v[86:89], v[88:89], v[44:45], v[108:111]
	s_nop 4
	v_max_f32_e32 v101, v91, v91
	s_nop 0
	v_max_f32_e32 v108, v90, v90
	v_max_f32_e32 v101, v108, v101
	v_max_f32_e32 v108, v93, v93
	v_max_f32_e32 v109, v92, v92
	v_max_f32_e32 v108, v109, v108
	v_max_f32_e32 v109, v89, v89
	v_max_f32_e32 v110, v88, v88
	v_max_f32_e32 v109, v110, v109
	v_max3_f32 v109, v86, v87, v109
	v_max3_f32 v101, v101, v108, v109
	v_mov_b32_e32 v108, v101
	s_nop 1
	v_permlane16_swap_b32_e32 v101, v108
	v_max_f32_e32 v101, v101, v108
	v_mov_b32_e32 v108, v101
	s_nop 1
	v_permlane32_swap_b32_e32 v101, v108
	v_max_f32_e32 v101, v101, v108
	v_cmp_gt_f32_e32 vcc, v101, v114
	s_cbranch_vccz .LBB0_763
	v_max_f32_e32 v101, v101, v101
	v_max_f32_e32 v108, v114, v114
	v_max_f32_e32 v101, v108, v101
	v_sub_f32_e32 v108, v114, v101
	v_exp_f32_e32 v108, v108
	v_mov_b32_e32 v114, v101
	v_mul_f32_e32 v115, v115, v108
	v_pk_mul_f32 v[20:21], v[20:21], v[108:109] op_sel_hi:[1,0]
	v_pk_mul_f32 v[18:19], v[18:19], v[108:109] op_sel_hi:[1,0]
	v_pk_mul_f32 v[16:17], v[16:17], v[108:109] op_sel_hi:[1,0]
	v_pk_mul_f32 v[14:15], v[14:15], v[108:109] op_sel_hi:[1,0]
	v_pk_mul_f32 v[12:13], v[12:13], v[108:109] op_sel_hi:[1,0]
	v_pk_mul_f32 v[10:11], v[10:11], v[108:109] op_sel_hi:[1,0]
	v_pk_mul_f32 v[8:9], v[8:9], v[108:109] op_sel_hi:[1,0]
	v_pk_mul_f32 v[6:7], v[6:7], v[108:109] op_sel_hi:[1,0]

.LBB0_766:
	s_lshl_b32 s6, s8, 13
	s_add_i32 s18, s6, 0x30000
	s_add_i32 s6, s0, -4
	s_ashr_i32 s15, s6, 1
	s_add_i32 s6, s15, 1
	s_lshl_b64 s[10:11], s[18:19], 6
	s_lshl_b32 s18, s7, 6
	s_max_i32 s7, s15, 0
	s_max_i32 s8, s6, 0
	s_lshl_b64 s[28:29], s[18:19], 14
	s_lshl_b32 s96, s7, 12
	s_lshl_b32 s60, s8, 12
	s_cmp_lt_u32 s15, 16
	s_cselect_b64 s[62:63], -1, 0
	s_lshl_b32 s7, s7, 11
	s_lshl_b32 s78, s15, 7
	s_add_i32 s76, s1, 0
	v_readlane_b32 s30, v255, 39
	v_readlane_b32 s31, v255, 40
	s_add_u32 s10, s30, s10
	s_addc_u32 s11, s31, s11
	v_readlane_b32 s30, v255, 60
	v_readlane_b32 s31, v255, 61
	s_add_u32 s30, s30, s28
	s_addc_u32 s31, s31, s29
	s_lshl_b32 s1, s69, 15
	s_waitcnt vmcnt(1)
	v_lshl_or_b32 v62, s0, 4, v149
	s_add_u32 s28, s10, s1
	v_lshlrev_b32_e32 v118, 4, v62
	s_addc_u32 s29, s11, 0
	s_lshl_b32 s1, s69, 16
	v_or_b32_e32 v2, s69, v118
	s_add_u32 s86, s30, s1
	v_mul_u32_u24_e32 v2, 0xf00, v2
	s_addc_u32 s87, s31, 0
	v_lshl_add_u64 v[38:39], s[92:93], 0, v[2:3]
	v_mov_b32_e32 v5, v3
	v_lshl_add_u64 v[38:39], v[38:39], 0, v[154:155]
	v_lshl_add_u64 v[40:41], s[86:87], 0, v[4:5]
	v_mov_b32_e32 v103, v3
	s_mov_b32 s61, s19
	v_lshl_add_u64 v[38:39], v[38:39], 0, s[64:65]
	v_lshl_add_u64 v[98:99], s[28:29], 0, v[154:155]
	v_lshl_add_u64 v[100:101], v[40:41], 0, v[102:103]
	v_lshl_or_b32 v110, s8, 11, v160
	v_mov_b32_e32 v111, v3
	v_lshl_add_u64 v[40:41], v[98:99], 0, v[110:111]
	global_load_dwordx4 v[46:49], v[38:39], off offset:2048 nt
	global_load_dwordx4 v[58:61], v[40:41], off
	v_lshl_add_u64 v[38:39], v[100:101], 0, s[60:61]
	global_load_dwordx4 v[66:69], v[40:41], off offset:1024
	global_load_dwordx4 v[54:57], v[38:39], off
	global_load_dwordx4 v[50:53], v[38:39], off offset:1024
	global_load_dwordx4 v[42:45], v[38:39], off offset:2048
	s_nop 0
	global_load_dwordx4 v[38:41], v[38:39], off offset:3072
	s_mov_b32 s97, s19
	s_cmp_gt_u32 s15, 15
	v_sub_u32_e32 v116, v153, v62
	v_or_b32_e32 v104, s7, v160
	s_cbranch_scc1 .LBB0_770
	v_mov_b32_e32 v105, v3
	v_lshl_add_u64 v[70:71], v[98:99], 0, v[104:105]
	global_load_dwordx4 v[62:65], v[70:71], off
	global_load_dwordx4 v[80:83], v[70:71], off offset:1024
	s_add_i32 s0, s76, s78
	v_lshl_add_u32 v2, v116, 2, s0
	v_add_u32_e32 v5, 0xa560, v2
	v_add_u32_e32 v72, 0xa568, v2
	ds_read2_b32 v[70:71], v5 offset1:1
	ds_read2_b32 v[72:73], v72 offset1:1
	v_add_u32_e32 v5, 0xa5a0, v2
	v_add_u32_e32 v2, 0xa5a8, v2
	ds_read2_b32 v[74:75], v5 offset1:1
	ds_read2_b32 v[76:77], v2 offset1:1
	s_waitcnt vmcnt(1) lgkmcnt(2)
	v_mfma_f32_16x16x32_fp8_fp8 v[70:73], v[62:63], v[46:47], v[70:73]
	v_lshl_add_u64 v[62:63], v[100:101], 0, s[96:97]
	s_waitcnt vmcnt(0) lgkmcnt(0)
	v_mfma_f32_16x16x32_fp8_fp8 v[90:93], v[80:81], v[46:47], v[74:77]
	global_load_dwordx4 v[78:81], v[62:63], off
	s_nop 1
	global_load_dwordx4 v[74:77], v[62:63], off offset:1024
	v_mfma_f32_16x16x32_fp8_fp8 v[86:89], v[64:65], v[48:49], v[70:73]
	s_nop 2
	global_load_dwordx4 v[70:73], v[62:63], off offset:2048
	s_nop 0
	global_load_dwordx4 v[62:65], v[62:63], off offset:3072
	s_nop 1
	v_max_f32_e32 v2, v87, v87
	v_mfma_f32_16x16x32_fp8_fp8 v[82:85], v[82:83], v[48:49], v[90:93]
	v_max_f32_e32 v5, v86, v86
	v_max_f32_e32 v2, v5, v2
	s_nop 0
	v_max_f32_e32 v90, v89, v89
	v_max_f32_e32 v91, v88, v88
	s_nop 2
	v_max_f32_e32 v92, v85, v85
	v_max_f32_e32 v93, v84, v84
	v_max_f32_e32 v5, v91, v90
	v_max_f32_e32 v90, v93, v92
	v_max3_f32 v90, v82, v83, v90
	v_max3_f32 v2, v2, v5, v90
	v_mov_b32_e32 v5, v2
	s_nop 1
	v_permlane16_swap_b32_e32 v2, v5
	v_max_f32_e32 v2, v2, v5
	v_mov_b32_e32 v5, v2
	s_nop 1
	v_permlane32_swap_b32_e32 v2, v5
	v_max_f32_e32 v2, v2, v5
	v_cmp_gt_f32_e32 vcc, v2, v112
	s_cbranch_vccz .LBB0_769
	v_max_f32_e32 v2, v2, v2
	v_max_f32_e32 v5, v112, v112
	v_max_f32_e32 v5, v5, v2
	v_sub_f32_e32 v2, v112, v5
	v_exp_f32_e32 v2, v2
	v_mov_b32_e32 v112, v5
	v_mul_f32_e32 v113, v113, v2
	v_pk_mul_f32 v[36:37], v[36:37], v[2:3] op_sel_hi:[1,0]
	v_pk_mul_f32 v[34:35], v[34:35], v[2:3] op_sel_hi:[1,0]
	v_pk_mul_f32 v[32:33], v[32:33], v[2:3] op_sel_hi:[1,0]
	v_pk_mul_f32 v[30:31], v[30:31], v[2:3] op_sel_hi:[1,0]
	v_pk_mul_f32 v[28:29], v[28:29], v[2:3] op_sel_hi:[1,0]
	v_pk_mul_f32 v[26:27], v[26:27], v[2:3] op_sel_hi:[1,0]
	v_pk_mul_f32 v[24:25], v[24:25], v[2:3] op_sel_hi:[1,0]
	v_pk_mul_f32 v[22:23], v[22:23], v[2:3] op_sel_hi:[1,0]

.LBB0_770:
	s_add_i32 s8, s15, 2
	s_lshl_b32 s28, s8, 12
	s_mov_b32 s29, s19
	v_lshl_or_b32 v106, s8, 11, v160
	v_mov_b32_e32 v107, v3
	v_lshl_add_u64 v[62:63], v[98:99], 0, v[106:107]
	v_lshl_add_u64 v[78:79], v[100:101], 0, s[28:29]
	global_load_dwordx4 v[94:97], v[62:63], off
	global_load_dwordx4 v[90:93], v[62:63], off offset:1024
	s_nop 0
	global_load_dwordx4 v[62:65], v[78:79], off
	global_load_dwordx4 v[70:73], v[78:79], off offset:1024
	global_load_dwordx4 v[74:77], v[78:79], off offset:2048
	s_nop 0
	global_load_dwordx4 v[78:81], v[78:79], off offset:3072
	s_cmp_lt_u32 s6, 16
	s_mov_b32 s35, s79
	s_cselect_b64 s[0:1], -1, 0
	s_lshl_b32 s79, s6, 7
	s_cmp_gt_u32 s6, 15
	s_cbranch_scc1 .LBB0_774
	s_add_i32 s6, s76, s79
	v_lshl_add_u32 v2, v116, 2, s6
	v_add_u32_e32 v5, 0xa560, v2
	v_add_u32_e32 v84, 0xa568, v2
	ds_read2_b32 v[82:83], v5 offset1:1
	ds_read2_b32 v[84:85], v84 offset1:1
	v_add_u32_e32 v5, 0xa5a0, v2
	v_add_u32_e32 v2, 0xa5a8, v2
	ds_read2_b32 v[86:87], v5 offset1:1
	ds_read2_b32 v[88:89], v2 offset1:1
	s_waitcnt vmcnt(11) lgkmcnt(2)
	v_mfma_f32_16x16x32_fp8_fp8 v[82:85], v[58:59], v[46:47], v[82:85]
	s_waitcnt vmcnt(10) lgkmcnt(0)
	v_mfma_f32_16x16x32_fp8_fp8 v[86:89], v[66:67], v[46:47], v[86:89]
	v_mfma_f32_16x16x32_fp8_fp8 v[82:85], v[60:61], v[48:49], v[82:85]
	v_mfma_f32_16x16x32_fp8_fp8 v[58:61], v[68:69], v[48:49], v[86:89]
	s_nop 6
	v_max_f32_e32 v2, v83, v83
	v_max_f32_e32 v5, v82, v82
	v_max_f32_e32 v66, v85, v85
	v_max_f32_e32 v2, v5, v2
	v_max_f32_e32 v5, v84, v84
	v_max_f32_e32 v5, v5, v66
	v_max_f32_e32 v66, v61, v61
	v_max_f32_e32 v67, v60, v60
	v_max_f32_e32 v66, v67, v66
	v_max3_f32 v66, v58, v59, v66
	v_max3_f32 v2, v2, v5, v66
	v_mov_b32_e32 v5, v2
	s_nop 1
	v_permlane16_swap_b32_e32 v2, v5
	v_max_f32_e32 v2, v2, v5
	v_mov_b32_e32 v5, v2
	s_nop 1
	v_permlane32_swap_b32_e32 v2, v5
	v_max_f32_e32 v2, v2, v5
	v_cmp_gt_f32_e32 vcc, v2, v112
	s_cbranch_vccz .LBB0_773
	v_max_f32_e32 v2, v2, v2
	v_max_f32_e32 v5, v112, v112
	v_max_f32_e32 v5, v5, v2
	v_sub_f32_e32 v2, v112, v5
	v_exp_f32_e32 v2, v2
	v_mov_b32_e32 v112, v5
	v_mul_f32_e32 v113, v113, v2
	v_pk_mul_f32 v[36:37], v[36:37], v[2:3] op_sel_hi:[1,0]
	v_pk_mul_f32 v[34:35], v[34:35], v[2:3] op_sel_hi:[1,0]
	v_pk_mul_f32 v[32:33], v[32:33], v[2:3] op_sel_hi:[1,0]
	v_pk_mul_f32 v[30:31], v[30:31], v[2:3] op_sel_hi:[1,0]
	v_pk_mul_f32 v[28:29], v[28:29], v[2:3] op_sel_hi:[1,0]
	v_pk_mul_f32 v[26:27], v[26:27], v[2:3] op_sel_hi:[1,0]
	v_pk_mul_f32 v[24:25], v[24:25], v[2:3] op_sel_hi:[1,0]
	v_pk_mul_f32 v[22:23], v[22:23], v[2:3] op_sel_hi:[1,0]

.LBB0_774:
	s_lshl_b32 s8, s8, 7
	s_add_i32 s8, s76, s8
	v_lshl_add_u32 v2, v116, 2, s8
	v_add_u32_e32 v5, 0xa560, v2
	s_waitcnt vmcnt(6)
	v_add_u32_e32 v40, 0xa568, v2
	ds_read2_b32 v[38:39], v5 offset1:1
	ds_read2_b32 v[40:41], v40 offset1:1
	s_add_i32 s77, s15, 3
	s_min_u32 s18, s77, 15
	s_lshl_b32 s6, s18, 12
	s_waitcnt vmcnt(5) lgkmcnt(0)
	v_mfma_f32_16x16x32_fp8_fp8 v[50:53], v[94:95], v[46:47], v[38:41]
	s_mov_b32 s7, s19
	v_lshl_or_b32 v108, s18, 11, v160
	v_mov_b32_e32 v109, v3
	v_add_u32_e32 v5, 0xa5a0, v2
	v_lshl_add_u64 v[54:55], v[98:99], 0, v[108:109]
	v_mfma_f32_16x16x32_fp8_fp8 v[94:97], v[96:97], v[48:49], v[50:53]
	v_add_u32_e32 v2, 0xa5a8, v2
	ds_read2_b32 v[42:43], v5 offset1:1
	ds_read2_b32 v[44:45], v2 offset1:1
	v_lshl_add_u64 v[50:51], v[100:101], 0, s[6:7]
	global_load_dwordx4 v[82:85], v[54:55], off
	global_load_dwordx4 v[86:89], v[54:55], off offset:1024
	global_load_dwordx4 v[66:69], v[50:51], off
	global_load_dwordx4 v[58:61], v[50:51], off offset:1024
	s_nop 0
	global_load_dwordx4 v[54:57], v[50:51], off offset:2048
	s_nop 0
	global_load_dwordx4 v[50:53], v[50:51], off offset:3072
	s_waitcnt vmcnt(10) lgkmcnt(0)
	v_mfma_f32_16x16x32_fp8_fp8 v[120:123], v[90:91], v[46:47], v[42:45]
	v_max_f32_e32 v2, v95, v95
	v_max_f32_e32 v5, v94, v94
	v_max_f32_e32 v2, v5, v2
	v_mfma_f32_16x16x32_fp8_fp8 v[90:93], v[92:93], v[48:49], v[120:123]
	v_max_f32_e32 v5, v97, v97
	v_max_f32_e32 v103, v96, v96
	v_max_f32_e32 v5, v103, v5
	s_nop 4
	v_max_f32_e32 v103, v93, v93
	v_max_f32_e32 v105, v92, v92
	v_max_f32_e32 v103, v105, v103
	v_max3_f32 v103, v90, v91, v103
	v_max3_f32 v2, v2, v5, v103
	v_mov_b32_e32 v5, v2
	s_nop 1
	v_permlane16_swap_b32_e32 v2, v5
	v_max_f32_e32 v2, v2, v5
	v_mov_b32_e32 v5, v2
	s_nop 1
	v_permlane32_swap_b32_e32 v2, v5
	v_max_f32_e32 v2, v2, v5
	v_cmp_gt_f32_e32 vcc, v2, v112
	s_cbranch_vccz .LBB0_776
	v_max_f32_e32 v2, v2, v2
	v_max_f32_e32 v5, v112, v112
	v_max_f32_e32 v5, v5, v2
	v_sub_f32_e32 v2, v112, v5
	v_exp_f32_e32 v2, v2
	v_mov_b32_e32 v112, v5
	v_mul_f32_e32 v113, v113, v2
	v_pk_mul_f32 v[36:37], v[36:37], v[2:3] op_sel_hi:[1,0]
	v_pk_mul_f32 v[34:35], v[34:35], v[2:3] op_sel_hi:[1,0]
	v_pk_mul_f32 v[32:33], v[32:33], v[2:3] op_sel_hi:[1,0]
	v_pk_mul_f32 v[30:31], v[30:31], v[2:3] op_sel_hi:[1,0]
	v_pk_mul_f32 v[28:29], v[28:29], v[2:3] op_sel_hi:[1,0]
	v_pk_mul_f32 v[26:27], v[26:27], v[2:3] op_sel_hi:[1,0]
	v_pk_mul_f32 v[24:25], v[24:25], v[2:3] op_sel_hi:[1,0]
	v_pk_mul_f32 v[22:23], v[22:23], v[2:3] op_sel_hi:[1,0]
.LBB0_776:
	v_sub_f32_e32 v2, v94, v112
	v_exp_f32_e32 v2, v2
	v_sub_f32_e32 v94, v95, v112
	v_exp_f32_e32 v94, v94
	v_sub_f32_e32 v95, v96, v112
	v_exp_f32_e32 v95, v95
	v_sub_f32_e32 v96, v97, v112
	v_exp_f32_e32 v96, v96
	v_sub_f32_e32 v90, v90, v112
	v_add_f32_e32 v5, 0, v2
	v_exp_f32_e32 v97, v90
	v_sub_f32_e32 v90, v91, v112
	v_add_f32_e32 v5, v94, v5
	v_exp_f32_e32 v103, v90
	v_sub_f32_e32 v90, v92, v112
	v_add_f32_e32 v5, v95, v5
	v_exp_f32_e32 v105, v90
	v_sub_f32_e32 v90, v93, v112
	v_add_f32_e32 v5, v96, v5
	v_exp_f32_e32 v93, v90
	v_add_f32_e32 v5, v97, v5
	s_add_i32 s8, s15, 4
	v_add_f32_e32 v5, v103, v5
	s_min_u32 s86, s8, 15
	v_add_f32_e32 v5, v105, v5
	v_add_f32_e32 v5, v93, v5
	v_cvt_pk_bf16_f32 v90, v2, v94
	v_cvt_pk_bf16_f32 v91, v95, v96
	v_cvt_pk_bf16_f32 v92, v97, v103
	v_cvt_pk_bf16_f32 v93, v105, v93
	v_lshl_or_b32 v2, s86, 11, v160
	s_lshl_b32 s18, s86, 12
	s_waitcnt vmcnt(9)
	v_mfma_f32_16x16x32_bf16 v[34:37], v[62:65], v[90:93], v[34:37]
	v_lshl_add_u64 v[62:63], v[98:99], 0, v[2:3]
	s_cmp_lt_i32 s15, 13
	s_cselect_b64 s[94:95], -1, 0
	s_waitcnt vmcnt(8)
	v_mfma_f32_16x16x32_bf16 v[30:33], v[70:73], v[90:93], v[30:33]
	s_lshl_b32 s77, s77, 7
	s_cmp_gt_i32 s15, 12
	v_add_f32_e32 v117, v113, v5
	s_waitcnt vmcnt(7)
	v_mfma_f32_16x16x32_bf16 v[26:29], v[74:77], v[90:93], v[26:29]
	s_waitcnt vmcnt(6)
	v_mfma_f32_16x16x32_bf16 v[22:25], v[78:81], v[90:93], v[22:25]
	global_load_dwordx4 v[90:93], v[62:63], off
	global_load_dwordx4 v[94:97], v[62:63], off offset:1024
	v_lshl_add_u64 v[62:63], v[100:101], 0, s[18:19]
	global_load_dwordx4 v[78:81], v[62:63], off
	global_load_dwordx4 v[74:77], v[62:63], off offset:1024
	global_load_dwordx4 v[70:73], v[62:63], off offset:2048
	s_nop 0
	global_load_dwordx4 v[62:65], v[62:63], off offset:3072
	s_cbranch_scc1 .LBB0_780
	s_add_i32 s86, s76, s77
	v_lshl_add_u32 v5, v116, 2, s86
	v_add_u32_e32 v98, 0xa560, v5
	v_add_u32_e32 v100, 0xa568, v5
	ds_read2_b32 v[98:99], v98 offset1:1
	ds_read2_b32 v[100:101], v100 offset1:1
	v_add_u32_e32 v103, 0xa5a0, v5
	v_add_u32_e32 v5, 0xa5a8, v5
	ds_read2_b32 v[120:121], v103 offset1:1
	ds_read2_b32 v[122:123], v5 offset1:1
	s_waitcnt vmcnt(11) lgkmcnt(2)
	v_mfma_f32_16x16x32_fp8_fp8 v[98:101], v[82:83], v[46:47], v[98:101]
	s_waitcnt vmcnt(10) lgkmcnt(0)
	v_mfma_f32_16x16x32_fp8_fp8 v[120:123], v[86:87], v[46:47], v[120:123]
	v_mfma_f32_16x16x32_fp8_fp8 v[98:101], v[84:85], v[48:49], v[98:101]
	v_mfma_f32_16x16x32_fp8_fp8 v[82:85], v[88:89], v[48:49], v[120:123]
	s_nop 6
	v_max_f32_e32 v5, v99, v99
	v_max_f32_e32 v86, v98, v98
	v_max_f32_e32 v87, v101, v101
	v_max_f32_e32 v5, v86, v5
	v_max_f32_e32 v86, v100, v100
	v_max_f32_e32 v86, v86, v87
	v_max_f32_e32 v87, v85, v85
	v_max_f32_e32 v88, v84, v84
	v_max_f32_e32 v87, v88, v87
	v_max3_f32 v87, v82, v83, v87
	v_max3_f32 v5, v5, v86, v87
	v_mov_b32_e32 v86, v5
	s_nop 1
	v_permlane16_swap_b32_e32 v5, v86
	v_max_f32_e32 v5, v5, v86
	v_mov_b32_e32 v86, v5
	s_nop 1
	v_permlane32_swap_b32_e32 v5, v86
	v_max_f32_e32 v5, v5, v86
	v_cmp_gt_f32_e32 vcc, v5, v112
	s_cbranch_vccz .LBB0_779
	v_max_f32_e32 v5, v5, v5
	v_max_f32_e32 v86, v112, v112
	v_max_f32_e32 v5, v86, v5
	v_sub_f32_e32 v86, v112, v5
	v_exp_f32_e32 v86, v86
	v_mov_b32_e32 v112, v5
	v_mul_f32_e32 v117, v117, v86
	v_pk_mul_f32 v[36:37], v[36:37], v[86:87] op_sel_hi:[1,0]
	v_pk_mul_f32 v[34:35], v[34:35], v[86:87] op_sel_hi:[1,0]
	v_pk_mul_f32 v[32:33], v[32:33], v[86:87] op_sel_hi:[1,0]
	v_pk_mul_f32 v[30:31], v[30:31], v[86:87] op_sel_hi:[1,0]
	v_pk_mul_f32 v[28:29], v[28:29], v[86:87] op_sel_hi:[1,0]
	v_pk_mul_f32 v[26:27], v[26:27], v[86:87] op_sel_hi:[1,0]
	v_pk_mul_f32 v[24:25], v[24:25], v[86:87] op_sel_hi:[1,0]
	v_pk_mul_f32 v[22:23], v[22:23], v[86:87] op_sel_hi:[1,0]

.LBB0_780:
	s_cmp_lt_i32 s15, 12
	s_cselect_b64 s[86:87], -1, 0
	s_lshl_b32 s8, s8, 7
	s_cmp_gt_i32 s15, 11
	s_cbranch_scc1 .LBB0_784
	s_add_i32 s15, s76, s8
	v_lshl_add_u32 v5, v116, 2, s15
	s_waitcnt vmcnt(6)
	v_add_u32_e32 v50, 0xa560, v5
	v_add_u32_e32 v52, 0xa568, v5
	ds_read2_b32 v[50:51], v50 offset1:1
	ds_read2_b32 v[52:53], v52 offset1:1
	v_add_u32_e32 v54, 0xa5a0, v5
	v_add_u32_e32 v5, 0xa5a8, v5
	ds_read2_b32 v[54:55], v54 offset1:1
	ds_read2_b32 v[56:57], v5 offset1:1
	s_waitcnt vmcnt(5) lgkmcnt(2)
	v_mfma_f32_16x16x32_fp8_fp8 v[50:53], v[90:91], v[46:47], v[50:53]
	s_waitcnt vmcnt(4) lgkmcnt(0)
	v_mfma_f32_16x16x32_fp8_fp8 v[54:57], v[94:95], v[46:47], v[54:57]
	v_mfma_f32_16x16x32_fp8_fp8 v[50:53], v[92:93], v[48:49], v[50:53]
	v_mfma_f32_16x16x32_fp8_fp8 v[46:49], v[96:97], v[48:49], v[54:57]
	s_nop 6
	v_max_f32_e32 v5, v51, v51
	v_max_f32_e32 v54, v50, v50
	v_max_f32_e32 v55, v53, v53
	v_max_f32_e32 v5, v54, v5
	v_max_f32_e32 v54, v52, v52
	v_max_f32_e32 v54, v54, v55
	v_max_f32_e32 v55, v49, v49
	v_max_f32_e32 v56, v48, v48
	v_max_f32_e32 v55, v56, v55
	v_max3_f32 v55, v46, v47, v55
	v_max3_f32 v5, v5, v54, v55
	v_mov_b32_e32 v54, v5
	s_nop 1
	v_permlane16_swap_b32_e32 v5, v54
	v_max_f32_e32 v5, v5, v54
	v_mov_b32_e32 v54, v5
	s_nop 1
	v_permlane32_swap_b32_e32 v5, v54
	v_max_f32_e32 v5, v5, v54
	v_cmp_gt_f32_e32 vcc, v5, v112
	s_cbranch_vccz .LBB0_783
	v_max_f32_e32 v5, v5, v5
	v_max_f32_e32 v54, v112, v112
	v_max_f32_e32 v5, v54, v5
	v_sub_f32_e32 v54, v112, v5
	v_exp_f32_e32 v54, v54
	v_mov_b32_e32 v112, v5
	v_mul_f32_e32 v117, v117, v54
	v_pk_mul_f32 v[36:37], v[36:37], v[54:55] op_sel_hi:[1,0]
	v_pk_mul_f32 v[34:35], v[34:35], v[54:55] op_sel_hi:[1,0]
	v_pk_mul_f32 v[32:33], v[32:33], v[54:55] op_sel_hi:[1,0]
	v_pk_mul_f32 v[30:31], v[30:31], v[54:55] op_sel_hi:[1,0]
	v_pk_mul_f32 v[28:29], v[28:29], v[54:55] op_sel_hi:[1,0]
	v_pk_mul_f32 v[26:27], v[26:27], v[54:55] op_sel_hi:[1,0]
	v_pk_mul_f32 v[24:25], v[24:25], v[54:55] op_sel_hi:[1,0]
	v_pk_mul_f32 v[22:23], v[22:23], v[54:55] op_sel_hi:[1,0]

.LBB0_784:
	s_or_b32 s15, s69, 8
	v_or_b32_e32 v5, s15, v118
	v_mul_u32_u24_e32 v46, 0xf00, v5
	v_mov_b32_e32 v47, v3
	v_lshl_add_u64 v[46:47], s[92:93], 0, v[46:47]
	s_lshl_b32 s92, s15, 15
	s_add_u32 s10, s10, s92
	s_addc_u32 s11, s11, 0
	v_lshl_add_u64 v[112:113], s[10:11], 0, v[154:155]
	s_lshl_b32 s10, s15, 16
	s_add_u32 s10, s30, s10
	s_addc_u32 s11, s31, 0
	v_mov_b32_e32 v5, v3
	v_lshl_add_u64 v[4:5], s[10:11], 0, v[4:5]
	v_mov_b32_e32 v103, v3
	v_lshl_add_u64 v[46:47], v[46:47], 0, v[154:155]
	v_lshl_add_u64 v[4:5], v[4:5], 0, v[102:103]
	v_lshl_add_u64 v[46:47], v[46:47], 0, s[64:65]
	s_waitcnt vmcnt(6)
	v_lshl_add_u64 v[50:51], v[112:113], 0, v[110:111]
	v_lshl_add_u64 v[52:53], v[4:5], 0, s[60:61]
	global_load_dwordx4 v[46:49], v[46:47], off offset:2048 nt
	s_nop 0
	global_load_dwordx4 v[66:69], v[50:51], off
	global_load_dwordx4 v[74:77], v[50:51], off offset:1024
	global_load_dwordx4 v[62:65], v[52:53], off
	global_load_dwordx4 v[58:61], v[52:53], off offset:1024
	global_load_dwordx4 v[54:57], v[52:53], off offset:2048
	s_nop 0
	global_load_dwordx4 v[50:53], v[52:53], off offset:3072
	s_andn2_b64 vcc, exec, s[62:63]
	s_cbranch_vccnz .LBB0_788
	v_mov_b32_e32 v105, v3
	s_waitcnt vmcnt(8)
	v_lshl_add_u64 v[70:71], v[4:5], 0, s[96:97]
	v_lshl_add_u64 v[90:91], v[112:113], 0, v[104:105]
	global_load_dwordx4 v[86:89], v[70:71], off
	global_load_dwordx4 v[82:85], v[70:71], off offset:1024
	global_load_dwordx4 v[78:81], v[70:71], off offset:2048
	s_nop 0
	global_load_dwordx4 v[70:73], v[70:71], off offset:3072
	s_nop 0
	global_load_dwordx4 v[94:97], v[90:91], off offset:1024
	s_nop 0
	global_load_dwordx4 v[90:93], v[90:91], off
	s_add_i32 s10, s76, s78
	v_lshl_add_u32 v98, v116, 2, s10
	v_add_u32_e32 v99, 0xa560, v98
	v_add_u32_e32 v100, 0xa568, v98
	v_add_u32_e32 v102, 0xa5a0, v98
	v_add_u32_e32 v104, 0xa5a8, v98
	ds_read2_b32 v[98:99], v99 offset1:1
	ds_read2_b32 v[100:101], v100 offset1:1
	ds_read2_b32 v[102:103], v102 offset1:1
	ds_read2_b32 v[104:105], v104 offset1:1
	s_waitcnt vmcnt(0) lgkmcnt(2)
	v_mfma_f32_16x16x32_fp8_fp8 v[98:101], v[90:91], v[46:47], v[98:101]
	v_mfma_f32_16x16x32_fp8_fp8 v[90:93], v[92:93], v[48:49], v[98:101]
	s_waitcnt lgkmcnt(0)
	v_mfma_f32_16x16x32_fp8_fp8 v[98:101], v[94:95], v[46:47], v[102:105]
	v_mfma_f32_16x16x32_fp8_fp8 v[94:97], v[96:97], v[48:49], v[98:101]
	s_nop 6
	v_max3_f32 v98, v90, v91, v92
	v_max_f32_e32 v98, v98, v93
	s_nop 3
	v_max3_f32 v100, v95, v96, v97
	v_max3_f32 v98, v98, v94, v100
	v_mov_b32_e32 v99, v98
	s_nop 1
	v_permlane16_swap_b32_e32 v98, v99
	v_max_f32_e32 v98, v98, v99
	v_mov_b32_e32 v99, v98
	s_nop 1
	v_permlane32_swap_b32_e32 v98, v99
	v_max_f32_e32 v98, v98, v99
	v_cmp_gt_f32_e32 vcc, v98, v114
	s_cbranch_vccz .LBB0_787
	v_max_f32_e32 v98, v98, v98
	v_max_f32_e32 v99, v114, v114
	v_max_f32_e32 v99, v99, v98
	v_sub_f32_e32 v98, v114, v99
	v_exp_f32_e32 v98, v98
	v_mov_b32_e32 v114, v99
	v_mul_f32_e32 v115, v115, v98
	v_pk_mul_f32 v[20:21], v[20:21], v[98:99] op_sel_hi:[1,0]
	v_pk_mul_f32 v[18:19], v[18:19], v[98:99] op_sel_hi:[1,0]
	v_pk_mul_f32 v[16:17], v[16:17], v[98:99] op_sel_hi:[1,0]
	v_pk_mul_f32 v[14:15], v[14:15], v[98:99] op_sel_hi:[1,0]
	v_pk_mul_f32 v[12:13], v[12:13], v[98:99] op_sel_hi:[1,0]
	v_pk_mul_f32 v[10:11], v[10:11], v[98:99] op_sel_hi:[1,0]
	v_pk_mul_f32 v[8:9], v[8:9], v[98:99] op_sel_hi:[1,0]
	v_pk_mul_f32 v[6:7], v[6:7], v[98:99] op_sel_hi:[1,0]

.LBB0_788:
	s_waitcnt vmcnt(8)
	v_lshl_add_u64 v[70:71], v[112:113], 0, v[106:107]
	v_lshl_add_u64 v[78:79], v[4:5], 0, s[28:29]
	global_load_dwordx4 v[98:101], v[70:71], off
	global_load_dwordx4 v[94:97], v[70:71], off offset:1024
	s_nop 0
	global_load_dwordx4 v[70:73], v[78:79], off
	global_load_dwordx4 v[82:85], v[78:79], off offset:1024
	global_load_dwordx4 v[86:89], v[78:79], off offset:2048
	global_load_dwordx4 v[90:93], v[78:79], off offset:3072
	s_andn2_b64 vcc, exec, s[0:1]
	s_cbranch_vccnz .LBB0_792
	s_add_i32 s0, s76, s79
	v_lshl_add_u32 v102, v116, 2, s0
	v_add_u32_e32 v78, 0xa560, v102
	v_add_u32_e32 v80, 0xa568, v102
	ds_read2_b32 v[78:79], v78 offset1:1
	ds_read2_b32 v[80:81], v80 offset1:1
	v_add_u32_e32 v103, 0xa5a0, v102
	v_add_u32_e32 v104, 0xa5a8, v102
	ds_read2_b32 v[102:103], v103 offset1:1
	ds_read2_b32 v[104:105], v104 offset1:1
	s_waitcnt vmcnt(11) lgkmcnt(2)
	v_mfma_f32_16x16x32_fp8_fp8 v[78:81], v[66:67], v[46:47], v[78:81]
	s_waitcnt vmcnt(10) lgkmcnt(0)
	v_mfma_f32_16x16x32_fp8_fp8 v[102:105], v[74:75], v[46:47], v[102:105]
	v_mfma_f32_16x16x32_fp8_fp8 v[78:81], v[68:69], v[48:49], v[78:81]
	v_mfma_f32_16x16x32_fp8_fp8 v[66:69], v[76:77], v[48:49], v[102:105]
	s_nop 6
	v_max_f32_e32 v74, v79, v79
	v_max_f32_e32 v75, v78, v78
	v_max_f32_e32 v76, v81, v81
	v_max_f32_e32 v74, v75, v74
	v_max_f32_e32 v75, v80, v80
	v_max_f32_e32 v75, v75, v76
	v_max_f32_e32 v76, v69, v69
	v_max_f32_e32 v77, v68, v68
	v_max_f32_e32 v76, v77, v76
	v_max3_f32 v76, v66, v67, v76
	v_max3_f32 v74, v74, v75, v76
	v_mov_b32_e32 v75, v74
	s_nop 1
	v_permlane16_swap_b32_e32 v74, v75
	v_max_f32_e32 v74, v74, v75
	v_mov_b32_e32 v75, v74
	s_nop 1
	v_permlane32_swap_b32_e32 v74, v75
	v_max_f32_e32 v74, v74, v75
	v_cmp_gt_f32_e32 vcc, v74, v114
	s_cbranch_vccz .LBB0_791
	v_max_f32_e32 v74, v74, v74
	v_max_f32_e32 v75, v114, v114
	v_max_f32_e32 v75, v75, v74
	v_sub_f32_e32 v74, v114, v75
	v_exp_f32_e32 v74, v74
	v_mov_b32_e32 v114, v75
	v_mul_f32_e32 v115, v115, v74
	v_pk_mul_f32 v[20:21], v[20:21], v[74:75] op_sel_hi:[1,0]
	v_pk_mul_f32 v[18:19], v[18:19], v[74:75] op_sel_hi:[1,0]
	v_pk_mul_f32 v[16:17], v[16:17], v[74:75] op_sel_hi:[1,0]
	v_pk_mul_f32 v[14:15], v[14:15], v[74:75] op_sel_hi:[1,0]
	v_pk_mul_f32 v[12:13], v[12:13], v[74:75] op_sel_hi:[1,0]
	v_pk_mul_f32 v[10:11], v[10:11], v[74:75] op_sel_hi:[1,0]
	v_pk_mul_f32 v[8:9], v[8:9], v[74:75] op_sel_hi:[1,0]
	v_pk_mul_f32 v[6:7], v[6:7], v[74:75] op_sel_hi:[1,0]

.LBB0_793:
	s_waitcnt vmcnt(5)
	v_mfma_f32_16x16x32_fp8_fp8 v[38:41], v[98:99], v[46:47], v[38:41]
	v_lshl_add_u64 v[50:51], v[112:113], 0, v[108:109]
	v_lshl_add_u64 v[62:63], v[4:5], 0, s[6:7]
	global_load_dwordx4 v[74:77], v[50:51], off
	global_load_dwordx4 v[78:81], v[50:51], off offset:1024
	global_load_dwordx4 v[66:69], v[62:63], off
	global_load_dwordx4 v[58:61], v[62:63], off offset:1024
	v_mfma_f32_16x16x32_fp8_fp8 v[54:57], v[100:101], v[48:49], v[38:41]
	global_load_dwordx4 v[50:53], v[62:63], off offset:2048
	s_nop 1
	global_load_dwordx4 v[38:41], v[62:63], off offset:3072
	v_readlane_b32 s35, v255, 44
	s_nop 2
	v_max_f32_e32 v62, v55, v55
	s_waitcnt vmcnt(10)
	v_mfma_f32_16x16x32_fp8_fp8 v[42:45], v[94:95], v[46:47], v[42:45]
	v_max_f32_e32 v63, v54, v54
	v_max_f32_e32 v62, v63, v62
	v_max_f32_e32 v63, v57, v57
	v_mfma_f32_16x16x32_fp8_fp8 v[42:45], v[96:97], v[48:49], v[42:45]
	v_max_f32_e32 v64, v56, v56
	v_max_f32_e32 v63, v64, v63
	s_nop 5
	v_max_f32_e32 v64, v45, v45
	v_max_f32_e32 v65, v44, v44
	v_max_f32_e32 v64, v65, v64
	v_max3_f32 v64, v42, v43, v64
	v_max3_f32 v62, v62, v63, v64
	v_mov_b32_e32 v63, v62
	s_nop 1
	v_permlane16_swap_b32_e32 v62, v63
	v_max_f32_e32 v62, v62, v63
	v_mov_b32_e32 v63, v62
	s_nop 1
	v_permlane32_swap_b32_e32 v62, v63
	v_max_f32_e32 v62, v62, v63
	v_cmp_gt_f32_e32 vcc, v62, v114
	s_cbranch_vccz .LBB0_795
	v_max_f32_e32 v62, v62, v62
	v_max_f32_e32 v63, v114, v114
	v_max_f32_e32 v63, v63, v62
	v_sub_f32_e32 v62, v114, v63
	v_exp_f32_e32 v62, v62
	v_mov_b32_e32 v114, v63
	v_mul_f32_e32 v115, v115, v62
	v_pk_mul_f32 v[20:21], v[20:21], v[62:63] op_sel_hi:[1,0]
	v_pk_mul_f32 v[18:19], v[18:19], v[62:63] op_sel_hi:[1,0]
	v_pk_mul_f32 v[16:17], v[16:17], v[62:63] op_sel_hi:[1,0]
	v_pk_mul_f32 v[14:15], v[14:15], v[62:63] op_sel_hi:[1,0]
	v_pk_mul_f32 v[12:13], v[12:13], v[62:63] op_sel_hi:[1,0]
	v_pk_mul_f32 v[10:11], v[10:11], v[62:63] op_sel_hi:[1,0]
	v_pk_mul_f32 v[8:9], v[8:9], v[62:63] op_sel_hi:[1,0]
	v_pk_mul_f32 v[6:7], v[6:7], v[62:63] op_sel_hi:[1,0]
.LBB0_795:
	v_sub_f32_e32 v54, v54, v114
	v_exp_f32_e32 v54, v54
	v_sub_f32_e32 v55, v55, v114
	v_exp_f32_e32 v55, v55
	v_sub_f32_e32 v56, v56, v114
	v_exp_f32_e32 v56, v56
	v_sub_f32_e32 v57, v57, v114
	v_exp_f32_e32 v57, v57
	v_sub_f32_e32 v42, v42, v114
	v_add_f32_e32 v62, 0, v54
	v_exp_f32_e32 v63, v42
	v_add_f32_e32 v62, v55, v62
	v_add_f32_e32 v62, v56, v62
	v_add_f32_e32 v62, v57, v62
	v_sub_f32_e32 v43, v43, v114
	v_add_f32_e32 v42, v63, v62
	v_exp_f32_e32 v62, v43
	v_sub_f32_e32 v43, v44, v114
	v_exp_f32_e32 v64, v43
	v_sub_f32_e32 v43, v45, v114
	v_exp_f32_e32 v45, v43
	v_add_f32_e32 v42, v62, v42
	v_add_f32_e32 v42, v64, v42
	v_cvt_pk_bf16_f32 v43, v56, v57
	v_add_f32_e32 v42, v45, v42
	v_add_f32_e32 v94, v115, v42
	v_cvt_pk_bf16_f32 v42, v54, v55
	v_cvt_pk_bf16_f32 v44, v63, v62
	v_cvt_pk_bf16_f32 v45, v64, v45
	v_lshl_add_u64 v[4:5], v[4:5], 0, s[18:19]
	s_andn2_b64 vcc, exec, s[94:95]
	s_waitcnt vmcnt(9)
	v_mfma_f32_16x16x32_bf16 v[18:21], v[70:73], v[42:45], v[18:21]
	s_waitcnt vmcnt(8)
	v_mfma_f32_16x16x32_bf16 v[14:17], v[82:85], v[42:45], v[14:17]
	s_waitcnt vmcnt(7)
	v_mfma_f32_16x16x32_bf16 v[10:13], v[86:89], v[42:45], v[10:13]
	s_waitcnt vmcnt(6)
	v_mfma_f32_16x16x32_bf16 v[6:9], v[90:93], v[42:45], v[6:9]
	v_lshl_add_u64 v[42:43], v[112:113], 0, v[2:3]
	global_load_dwordx4 v[82:85], v[42:43], off
	global_load_dwordx4 v[86:89], v[42:43], off offset:1024
	global_load_dwordx4 v[70:73], v[4:5], off
	global_load_dwordx4 v[62:65], v[4:5], off offset:1024
	global_load_dwordx4 v[54:57], v[4:5], off offset:2048
	s_nop 0
	global_load_dwordx4 v[42:45], v[4:5], off offset:3072
	s_cbranch_vccnz .LBB0_799
	s_add_i32 s0, s76, s77
	v_lshl_add_u32 v2, v116, 2, s0
	v_add_u32_e32 v4, 0xa560, v2
	v_add_u32_e32 v5, 0xa568, v2
	ds_read2_b32 v[90:91], v4 offset1:1
	ds_read2_b32 v[92:93], v5 offset1:1
	v_add_u32_e32 v4, 0xa5a0, v2
	v_add_u32_e32 v2, 0xa5a8, v2
	ds_read2_b32 v[96:97], v4 offset1:1
	ds_read2_b32 v[98:99], v2 offset1:1
	s_waitcnt vmcnt(11) lgkmcnt(2)
	v_mfma_f32_16x16x32_fp8_fp8 v[90:93], v[74:75], v[46:47], v[90:93]
	s_waitcnt vmcnt(10) lgkmcnt(0)
	v_mfma_f32_16x16x32_fp8_fp8 v[96:99], v[78:79], v[46:47], v[96:99]
	v_mfma_f32_16x16x32_fp8_fp8 v[90:93], v[76:77], v[48:49], v[90:93]
	v_mfma_f32_16x16x32_fp8_fp8 v[74:77], v[80:81], v[48:49], v[96:99]
	s_nop 6
	v_max_f32_e32 v2, v91, v91
	v_max_f32_e32 v4, v90, v90
	v_max_f32_e32 v5, v93, v93
	v_max_f32_e32 v2, v4, v2
	v_max_f32_e32 v4, v92, v92
	v_max_f32_e32 v4, v4, v5
	v_max_f32_e32 v5, v77, v77
	v_max_f32_e32 v78, v76, v76
	v_max_f32_e32 v5, v78, v5
	v_max3_f32 v5, v74, v75, v5
	v_max3_f32 v2, v2, v4, v5
	v_mov_b32_e32 v4, v2
	s_nop 1
	v_permlane16_swap_b32_e32 v2, v4
	v_max_f32_e32 v2, v2, v4
	v_mov_b32_e32 v4, v2
	s_nop 1
	v_permlane32_swap_b32_e32 v2, v4
	v_max_f32_e32 v2, v2, v4
	v_cmp_gt_f32_e32 vcc, v2, v114
	s_cbranch_vccz .LBB0_798
	v_max_f32_e32 v2, v2, v2
	v_max_f32_e32 v4, v114, v114
	v_max_f32_e32 v4, v4, v2
	v_sub_f32_e32 v2, v114, v4
	v_exp_f32_e32 v2, v2
	v_mov_b32_e32 v114, v4
	v_mul_f32_e32 v94, v94, v2
	v_pk_mul_f32 v[20:21], v[20:21], v[2:3] op_sel_hi:[1,0]
	v_pk_mul_f32 v[18:19], v[18:19], v[2:3] op_sel_hi:[1,0]
	v_pk_mul_f32 v[16:17], v[16:17], v[2:3] op_sel_hi:[1,0]
	v_pk_mul_f32 v[14:15], v[14:15], v[2:3] op_sel_hi:[1,0]
	v_pk_mul_f32 v[12:13], v[12:13], v[2:3] op_sel_hi:[1,0]
	v_pk_mul_f32 v[10:11], v[10:11], v[2:3] op_sel_hi:[1,0]
	v_pk_mul_f32 v[8:9], v[8:9], v[2:3] op_sel_hi:[1,0]
	v_pk_mul_f32 v[6:7], v[6:7], v[2:3] op_sel_hi:[1,0]

.LBB0_799:
	s_andn2_b64 vcc, exec, s[86:87]
	s_cbranch_vccnz .LBB0_803
	s_add_i32 s76, s76, s8
	v_lshl_add_u32 v2, v116, 2, s76
	v_add_u32_e32 v4, 0xa560, v2
	v_add_u32_e32 v5, 0xa568, v2
	s_waitcnt vmcnt(6)
	ds_read2_b32 v[38:39], v4 offset1:1
	ds_read2_b32 v[40:41], v5 offset1:1
	v_add_u32_e32 v4, 0xa5a0, v2
	v_add_u32_e32 v2, 0xa5a8, v2
	ds_read2_b32 v[50:51], v4 offset1:1
	ds_read2_b32 v[52:53], v2 offset1:1
	s_waitcnt vmcnt(5) lgkmcnt(2)
	v_mfma_f32_16x16x32_fp8_fp8 v[38:41], v[82:83], v[46:47], v[38:41]
	s_waitcnt vmcnt(4) lgkmcnt(0)
	v_mfma_f32_16x16x32_fp8_fp8 v[58:61], v[86:87], v[46:47], v[50:53]
	v_mfma_f32_16x16x32_fp8_fp8 v[50:53], v[84:85], v[48:49], v[38:41]
	v_mfma_f32_16x16x32_fp8_fp8 v[38:41], v[88:89], v[48:49], v[58:61]
	s_nop 6
	v_max_f32_e32 v2, v51, v51
	v_max_f32_e32 v4, v50, v50
	v_max_f32_e32 v5, v53, v53
	v_max_f32_e32 v2, v4, v2
	v_max_f32_e32 v4, v52, v52
	v_max_f32_e32 v4, v4, v5
	v_max_f32_e32 v5, v41, v41
	v_max_f32_e32 v46, v40, v40
	v_max_f32_e32 v5, v46, v5
	v_max3_f32 v5, v38, v39, v5
	v_max3_f32 v2, v2, v4, v5
	v_mov_b32_e32 v4, v2
	s_nop 1
	v_permlane16_swap_b32_e32 v2, v4
	v_max_f32_e32 v2, v2, v4
	v_mov_b32_e32 v4, v2
	s_nop 1
	v_permlane32_swap_b32_e32 v2, v4
	v_max_f32_e32 v2, v2, v4
	v_cmp_gt_f32_e32 vcc, v2, v114
	s_cbranch_vccz .LBB0_802
	v_max_f32_e32 v2, v2, v2
	v_max_f32_e32 v4, v114, v114
	v_max_f32_e32 v4, v4, v2
	v_sub_f32_e32 v2, v114, v4
	v_exp_f32_e32 v2, v2
	v_mov_b32_e32 v114, v4
	v_mul_f32_e32 v94, v94, v2
	v_pk_mul_f32 v[20:21], v[20:21], v[2:3] op_sel_hi:[1,0]
	v_pk_mul_f32 v[18:19], v[18:19], v[2:3] op_sel_hi:[1,0]
	v_pk_mul_f32 v[16:17], v[16:17], v[2:3] op_sel_hi:[1,0]
	v_pk_mul_f32 v[14:15], v[14:15], v[2:3] op_sel_hi:[1,0]
	v_pk_mul_f32 v[12:13], v[12:13], v[2:3] op_sel_hi:[1,0]
	v_pk_mul_f32 v[10:11], v[10:11], v[2:3] op_sel_hi:[1,0]
	v_pk_mul_f32 v[8:9], v[8:9], v[2:3] op_sel_hi:[1,0]
	v_pk_mul_f32 v[6:7], v[6:7], v[2:3] op_sel_hi:[1,0]

.LBB0_806:
	s_min_u32 s8, s7, 8
	s_add_i32 s8, s8, s6
	v_med3_i32 v5, s8, 0, v184
	v_lshl_or_b32 v2, v5, 11, v160
	v_lshl_add_u64 v[94:95], v[172:173], 0, v[2:3]
	v_lshlrev_b32_e32 v2, 12, v5
	v_lshl_add_u64 v[122:123], v[174:175], 0, v[2:3]
	global_load_dwordx4 v[90:93], v[94:95], off
	s_nop 0
	global_load_dwordx4 v[94:97], v[94:95], off offset:1024
	s_nop 0
	global_load_dwordx4 v[106:109], v[122:123], off
	global_load_dwordx4 v[110:113], v[122:123], off offset:1024
	global_load_dwordx4 v[118:121], v[122:123], off offset:2048
	s_nop 0
	global_load_dwordx4 v[122:125], v[122:123], off offset:3072
	s_add_i32 s8, s6, s7
	s_add_i32 s8, s8, -1
	s_cmpk_gt_u32 s8, 0xff
	s_cbranch_scc1 .LBB0_816
	ds_read2_b32 v[134:135], v190 offset1:1
	ds_read2_b32 v[136:137], v190 offset0:2 offset1:3
	ds_read2_b32 v[192:193], v190 offset0:16 offset1:17
	ds_read2_b32 v[194:195], v190 offset0:18 offset1:19
	s_waitcnt vmcnt(11) lgkmcnt(2)
	v_mfma_f32_16x16x32_fp8_fp8 v[134:137], v[130:131], v[70:71], v[134:137]
	v_mfma_f32_16x16x32_fp8_fp8 v[138:141], v[132:133], v[72:73], v[134:137]
	s_waitcnt vmcnt(10) lgkmcnt(0)
	v_mfma_f32_16x16x32_fp8_fp8 v[134:137], v[126:127], v[70:71], v[192:195]
	v_mfma_f32_16x16x32_fp8_fp8 v[134:137], v[128:129], v[72:73], v[134:137]
	s_nop 4
	v_max3_f32 v2, v138, v139, v140
	v_max_f32_e32 v2, v2, v141
	s_nop 3
	v_max3_f32 v191, v135, v136, v137
	v_max3_f32 v2, v2, v134, v191
	v_mov_b32_e32 v5, v2
	s_nop 1
	v_permlane16_swap_b32_e32 v2, v5
	v_max_f32_e32 v2, v2, v5
	v_mov_b32_e32 v5, v2
	s_nop 1
	v_permlane32_swap_b32_e32 v2, v5
	v_max_f32_e32 v2, v2, v5
	v_cmp_gt_f32_e32 vcc, v2, v176
	s_cbranch_vccz .LBB0_809
	v_max_f32_e32 v2, v2, v2
	v_max_f32_e32 v5, v176, v176
	v_max_f32_e32 v5, v5, v2
	v_sub_f32_e32 v2, v176, v5
	v_exp_f32_e32 v2, v2
	v_mov_b32_e32 v176, v5
	v_mul_f32_e32 v4, v4, v2
	v_pk_mul_f32 v[68:69], v[68:69], v[2:3] op_sel_hi:[1,0]
	v_pk_mul_f32 v[66:67], v[66:67], v[2:3] op_sel_hi:[1,0]
	v_pk_mul_f32 v[64:65], v[64:65], v[2:3] op_sel_hi:[1,0]
	v_pk_mul_f32 v[62:63], v[62:63], v[2:3] op_sel_hi:[1,0]
	v_pk_mul_f32 v[60:61], v[60:61], v[2:3] op_sel_hi:[1,0]
	v_pk_mul_f32 v[58:59], v[58:59], v[2:3] op_sel_hi:[1,0]
	v_pk_mul_f32 v[56:57], v[56:57], v[2:3] op_sel_hi:[1,0]
	v_pk_mul_f32 v[54:55], v[54:55], v[2:3] op_sel_hi:[1,0]
.LBB0_809:
	v_sub_f32_e32 v134, v134, v176
	v_exp_f32_e32 v193, v134
	v_sub_f32_e32 v134, v135, v176
	v_sub_f32_e32 v2, v138, v176
	v_sub_f32_e32 v138, v140, v176
	v_exp_f32_e32 v194, v134
	v_sub_f32_e32 v134, v136, v176
	v_sub_f32_e32 v5, v139, v176
	v_exp_f32_e32 v191, v138
	v_sub_f32_e32 v138, v141, v176
	v_exp_f32_e32 v195, v134
	v_sub_f32_e32 v134, v137, v176
	v_exp_f32_e32 v2, v2
	v_exp_f32_e32 v5, v5
	v_exp_f32_e32 v192, v138
	v_exp_f32_e32 v196, v134
	v_cvt_pk_bf16_f32 v136, v193, v194
	v_cvt_pk_bf16_f32 v134, v2, v5
	v_cvt_pk_bf16_f32 v135, v191, v192
	v_cvt_pk_bf16_f32 v137, v195, v196
	s_waitcnt vmcnt(9)
	s_nop 0
	v_mfma_f32_16x16x32_bf16 v[66:69], v[114:117], v[134:137], v[66:69]
	s_waitcnt vmcnt(8)
	v_mfma_f32_16x16x32_bf16 v[62:65], v[102:105], v[134:137], v[62:65]
	s_waitcnt vmcnt(7)
	v_mfma_f32_16x16x32_bf16 v[58:61], v[98:101], v[134:137], v[58:61]
	s_waitcnt vmcnt(6)
	v_mfma_f32_16x16x32_bf16 v[54:57], v[86:89], v[134:137], v[54:57]
	v_add_u32_e32 v134, 0x504, v190
	v_add_u32_e32 v136, 0x50c, v190
	ds_read2_b32 v[134:135], v134 offset1:1
	ds_read2_b32 v[136:137], v136 offset1:1
	v_add_u32_e32 v138, 0x544, v190
	ds_read2_b32 v[198:199], v138 offset1:1
	v_add_u32_e32 v138, 0x54c, v190
	ds_read2_b32 v[200:201], v138 offset1:1
	s_waitcnt lgkmcnt(2)
	v_mfma_f32_16x16x32_fp8_fp8 v[134:137], v[130:131], v[74:75], v[134:137]
	v_mfma_f32_16x16x32_fp8_fp8 v[138:141], v[132:133], v[76:77], v[134:137]
	s_waitcnt lgkmcnt(0)
	v_mfma_f32_16x16x32_fp8_fp8 v[134:137], v[126:127], v[74:75], v[198:201]
	v_mfma_f32_16x16x32_fp8_fp8 v[134:137], v[128:129], v[76:77], v[134:137]
	s_nop 4
	v_max3_f32 v197, v138, v139, v140
	v_max_f32_e32 v197, v197, v141
	s_nop 3
	v_max3_f32 v199, v135, v136, v137
	v_max3_f32 v197, v197, v134, v199
	v_mov_b32_e32 v198, v197
	s_nop 1
	v_permlane16_swap_b32_e32 v197, v198
	v_max_f32_e32 v197, v197, v198
	v_mov_b32_e32 v198, v197
	s_nop 1
	v_permlane32_swap_b32_e32 v197, v198
	v_max_f32_e32 v197, v197, v198
	v_cmp_gt_f32_e32 vcc, v197, v177
	s_cbranch_vccz .LBB0_811
	v_max_f32_e32 v197, v197, v197
	v_max_f32_e32 v198, v177, v177
	v_max_f32_e32 v197, v198, v197
	v_sub_f32_e32 v177, v177, v197
	v_exp_f32_e32 v198, v177
	v_mov_b32_e32 v177, v197
	v_mul_f32_e32 v189, v189, v198
	v_pk_mul_f32 v[52:53], v[52:53], v[198:199] op_sel_hi:[1,0]
	v_pk_mul_f32 v[50:51], v[50:51], v[198:199] op_sel_hi:[1,0]
	v_pk_mul_f32 v[48:49], v[48:49], v[198:199] op_sel_hi:[1,0]
	v_pk_mul_f32 v[46:47], v[46:47], v[198:199] op_sel_hi:[1,0]
	v_pk_mul_f32 v[44:45], v[44:45], v[198:199] op_sel_hi:[1,0]
	v_pk_mul_f32 v[42:43], v[42:43], v[198:199] op_sel_hi:[1,0]
	v_pk_mul_f32 v[40:41], v[40:41], v[198:199] op_sel_hi:[1,0]
	v_pk_mul_f32 v[38:39], v[38:39], v[198:199] op_sel_hi:[1,0]
.LBB0_811:
	v_sub_f32_e32 v138, v138, v177
	v_sub_f32_e32 v134, v134, v177
	v_exp_f32_e32 v197, v138
	v_sub_f32_e32 v138, v139, v177
	v_exp_f32_e32 v201, v134
	v_sub_f32_e32 v134, v135, v177
	v_exp_f32_e32 v198, v138
	v_sub_f32_e32 v138, v140, v177
	v_exp_f32_e32 v202, v134
	v_sub_f32_e32 v134, v136, v177
	v_exp_f32_e32 v199, v138
	v_sub_f32_e32 v138, v141, v177
	v_exp_f32_e32 v203, v134
	v_sub_f32_e32 v134, v137, v177
	v_exp_f32_e32 v200, v138
	v_exp_f32_e32 v204, v134
	v_cvt_pk_bf16_f32 v134, v197, v198
	v_cvt_pk_bf16_f32 v136, v201, v202
	v_cvt_pk_bf16_f32 v135, v199, v200
	v_cvt_pk_bf16_f32 v137, v203, v204
	s_nop 1
	v_mfma_f32_16x16x32_bf16 v[50:53], v[114:117], v[134:137], v[50:53]
	v_mfma_f32_16x16x32_bf16 v[46:49], v[102:105], v[134:137], v[46:49]
	v_mfma_f32_16x16x32_bf16 v[42:45], v[98:101], v[134:137], v[42:45]
	v_mfma_f32_16x16x32_bf16 v[38:41], v[86:89], v[134:137], v[38:41]
	v_add_u32_e32 v134, 0xa08, v190
	v_add_u32_e32 v136, 0xa10, v190
	ds_read2_b32 v[134:135], v134 offset1:1
	ds_read2_b32 v[136:137], v136 offset1:1
	v_add_u32_e32 v138, 0xa48, v190
	ds_read2_b32 v[206:207], v138 offset1:1
	v_add_u32_e32 v138, 0xa50, v190
	ds_read2_b32 v[208:209], v138 offset1:1
	s_waitcnt lgkmcnt(2)
	v_mfma_f32_16x16x32_fp8_fp8 v[134:137], v[130:131], v[78:79], v[134:137]
	v_mfma_f32_16x16x32_fp8_fp8 v[138:141], v[132:133], v[80:81], v[134:137]
	s_waitcnt lgkmcnt(0)
	v_mfma_f32_16x16x32_fp8_fp8 v[134:137], v[126:127], v[78:79], v[206:209]
	v_mfma_f32_16x16x32_fp8_fp8 v[134:137], v[128:129], v[80:81], v[134:137]
	s_nop 4
	v_max3_f32 v205, v138, v139, v140
	v_max_f32_e32 v205, v205, v141
	s_nop 3
	v_max3_f32 v207, v135, v136, v137
	v_max3_f32 v205, v205, v134, v207
	v_mov_b32_e32 v206, v205
	s_nop 1
	v_permlane16_swap_b32_e32 v205, v206
	v_max_f32_e32 v205, v205, v206
	v_mov_b32_e32 v206, v205
	s_nop 1
	v_permlane32_swap_b32_e32 v205, v206
	v_max_f32_e32 v205, v205, v206
	v_cmp_gt_f32_e32 vcc, v205, v178
	s_cbranch_vccz .LBB0_813
	v_max_f32_e32 v205, v205, v205
	v_max_f32_e32 v206, v178, v178
	v_max_f32_e32 v205, v206, v205
	v_sub_f32_e32 v178, v178, v205
	v_exp_f32_e32 v178, v178
	s_nop 0
	v_mul_f32_e32 v188, v188, v178
	v_pk_mul_f32 v[36:37], v[36:37], v[178:179] op_sel_hi:[1,0]
	v_pk_mul_f32 v[34:35], v[34:35], v[178:179] op_sel_hi:[1,0]
	v_pk_mul_f32 v[32:33], v[32:33], v[178:179] op_sel_hi:[1,0]
	v_pk_mul_f32 v[30:31], v[30:31], v[178:179] op_sel_hi:[1,0]
	v_pk_mul_f32 v[28:29], v[28:29], v[178:179] op_sel_hi:[1,0]
	v_pk_mul_f32 v[26:27], v[26:27], v[178:179] op_sel_hi:[1,0]
	v_pk_mul_f32 v[24:25], v[24:25], v[178:179] op_sel_hi:[1,0]
	v_pk_mul_f32 v[22:23], v[22:23], v[178:179] op_sel_hi:[1,0]
	v_mov_b32_e32 v178, v205
.LBB0_813:
	v_sub_f32_e32 v138, v138, v178
	v_sub_f32_e32 v139, v139, v178
	v_sub_f32_e32 v140, v140, v178
	v_sub_f32_e32 v141, v141, v178
	v_sub_f32_e32 v134, v134, v178
	v_sub_f32_e32 v135, v135, v178
	v_sub_f32_e32 v136, v136, v178
	v_sub_f32_e32 v137, v137, v178
	v_exp_f32_e32 v138, v138
	v_exp_f32_e32 v139, v139
	v_exp_f32_e32 v140, v140
	v_exp_f32_e32 v141, v141
	v_exp_f32_e32 v134, v134
	v_exp_f32_e32 v135, v135
	v_exp_f32_e32 v136, v136
	v_exp_f32_e32 v137, v137
	v_cvt_pk_bf16_f32 v206, v138, v139
	v_cvt_pk_bf16_f32 v207, v140, v141
	v_cvt_pk_bf16_f32 v208, v134, v135
	v_cvt_pk_bf16_f32 v209, v136, v137
	s_nop 1
	v_mfma_f32_16x16x32_bf16 v[34:37], v[114:117], v[206:209], v[34:37]
	v_mfma_f32_16x16x32_bf16 v[30:33], v[102:105], v[206:209], v[30:33]
	v_mfma_f32_16x16x32_bf16 v[26:29], v[98:101], v[206:209], v[26:29]
	v_mfma_f32_16x16x32_bf16 v[22:25], v[86:89], v[206:209], v[22:25]
	v_add_u32_e32 v205, 0xf0c, v190
	v_add_u32_e32 v208, 0xf14, v190
	ds_read2_b32 v[206:207], v205 offset1:1
	ds_read2_b32 v[208:209], v208 offset1:1
	v_add_u32_e32 v205, 0xf4c, v190
	v_add_u32_e32 v212, 0xf54, v190
	ds_read2_b32 v[210:211], v205 offset1:1
	ds_read2_b32 v[212:213], v212 offset1:1
	s_waitcnt lgkmcnt(2)
	v_mfma_f32_16x16x32_fp8_fp8 v[206:209], v[130:131], v[82:83], v[206:209]
	s_waitcnt lgkmcnt(0)
	v_mfma_f32_16x16x32_fp8_fp8 v[210:213], v[126:127], v[82:83], v[210:213]
	v_mfma_f32_16x16x32_fp8_fp8 v[130:133], v[132:133], v[84:85], v[206:209]
	v_mfma_f32_16x16x32_fp8_fp8 v[126:129], v[128:129], v[84:85], v[210:213]
	s_nop 6
	v_max_f32_e32 v205, v131, v131
	v_max_f32_e32 v206, v130, v130
	v_max_f32_e32 v207, v133, v133
	v_max_f32_e32 v205, v206, v205
	v_max_f32_e32 v206, v132, v132
	v_max_f32_e32 v206, v206, v207
	v_max_f32_e32 v207, v129, v129
	v_max_f32_e32 v208, v128, v128
	v_max_f32_e32 v207, v208, v207
	v_max3_f32 v207, v126, v127, v207
	v_max3_f32 v205, v205, v206, v207
	v_mov_b32_e32 v206, v205
	s_nop 1
	v_permlane16_swap_b32_e32 v205, v206
	v_max_f32_e32 v205, v205, v206
	v_mov_b32_e32 v206, v205
	s_nop 1
	v_permlane32_swap_b32_e32 v205, v206
	v_max_f32_e32 v205, v205, v206
	v_cmp_gt_f32_e32 vcc, v205, v179
	s_cbranch_vccz .LBB0_815
	v_max_f32_e32 v205, v205, v205
	v_max_f32_e32 v206, v179, v179
	v_max_f32_e32 v205, v206, v205
	v_sub_f32_e32 v179, v179, v205
	v_exp_f32_e32 v206, v179
	v_mov_b32_e32 v179, v205
	v_mul_f32_e32 v187, v187, v206
	v_pk_mul_f32 v[20:21], v[20:21], v[206:207] op_sel_hi:[1,0]
	v_pk_mul_f32 v[18:19], v[18:19], v[206:207] op_sel_hi:[1,0]
	v_pk_mul_f32 v[16:17], v[16:17], v[206:207] op_sel_hi:[1,0]
	v_pk_mul_f32 v[14:15], v[14:15], v[206:207] op_sel_hi:[1,0]
	v_pk_mul_f32 v[12:13], v[12:13], v[206:207] op_sel_hi:[1,0]
	v_pk_mul_f32 v[10:11], v[10:11], v[206:207] op_sel_hi:[1,0]
	v_pk_mul_f32 v[8:9], v[8:9], v[206:207] op_sel_hi:[1,0]
	v_pk_mul_f32 v[6:7], v[6:7], v[206:207] op_sel_hi:[1,0]
